# RWKV scanner rewritten with the state update re-associated (S*w + kk*v issued in the DPP wait slots, single fma after the cross-lane reduction); same f32 ops
# speedup vs baseline: 1.0003x; 1.0003x over previous
.LBB0_512:
	s_and_b64 vcc, exec, s[6:7]
	s_cbranch_vccz .LBB0_482
	s_cmpk_eq_i32 s60, 0x80
	s_cbranch_scc1 .LBB0_483
	s_setprio 2
	s_mul_i32 s7, s60, 0xab
	s_bfe_u32 s7, s7, 0x70009
	s_and_b32 s6, s60, 1
	s_mul_i32 s7, s7, 3
	s_sub_i32 s7, s60, s7
	s_mul_i32 s8, s6, 0x2080
	s_and_b32 s7, s7, 0xff
	s_waitcnt vmcnt(0)
	v_add_u32_e32 v149, s8, v104
	v_lshl_add_u32 v80, s6, 15, v92
	v_lshl_add_u32 v81, s7, 12, v148
	v_lshl_add_u32 v2, s6, 12, v95
	ds_write2_b64 v149, v[70:71], v[72:73] offset1:1
	ds_write2_b32 v149, v74, v75 offset0:65 offset1:66
	ds_write2_b32 v149, v76, v77 offset0:67 offset1:68
	ds_read_b128 v[38:41], v80 offset:0
	ds_read_b128 v[42:45], v80 offset:256
	ds_read_b128 v[46:49], v80 offset:512
	ds_read_b128 v[50:53], v80 offset:768
	ds_read_b64 v[54:55], v81 offset:0
	ds_read_b128 v[56:59], v80 offset:1024
	ds_read_b128 v[150:153], v80 offset:1280
	ds_read_b128 v[154:157], v80 offset:1536
	ds_read_b128 v[158:161], v80 offset:1792
	ds_read_b64 v[60:61], v81 offset:128
	s_waitcnt lgkmcnt(5)
	ds_read_b64 v[78:79], v81 offset:256
	v_pk_mul_f32 v[178:179], v[72:73], v[40:41]
	v_pk_mul_f32 v[180:181], v[76:77], v[40:41]
	v_pk_fma_f32 v[178:179], v[70:71], v[38:39], v[178:179]
	v_pk_fma_f32 v[180:181], v[74:75], v[38:39], v[180:181]
	v_add_f32_e32 v182, v178, v179
	v_add_f32_e32 v183, v180, v181
	v_pk_mul_f32 v[72:73], v[72:73], v[44:45]
	v_pk_mul_f32 v[76:77], v[76:77], v[44:45]
	v_add_f32_dpp v182, v182, v182 row_ror:8 row_mask:0xf bank_mask:0xf bound_ctrl:1
	v_add_f32_dpp v183, v183, v183 row_ror:8 row_mask:0xf bank_mask:0xf bound_ctrl:1
	v_pk_mul_f32 v[70:71], v[70:71], v[42:43]
	v_pk_mul_f32 v[74:75], v[74:75], v[42:43]
	v_add_f32_dpp v182, v182, v182 row_ror:4 row_mask:0xf bank_mask:0xf bound_ctrl:1
	v_add_f32_dpp v183, v183, v183 row_ror:4 row_mask:0xf bank_mask:0xf bound_ctrl:1
	v_pk_fma_f32 v[72:73], v[52:53], v[54:55], v[72:73] op_sel_hi:[1,0,1]
	v_pk_fma_f32 v[76:77], v[52:53], v[54:55], v[76:77] op_sel:[0,1,0]
	v_add_f32_dpp v182, v182, v182 row_ror:2 row_mask:0xf bank_mask:0xf bound_ctrl:1
	v_add_f32_dpp v183, v183, v183 row_ror:2 row_mask:0xf bank_mask:0xf bound_ctrl:1
	v_pk_fma_f32 v[70:71], v[50:51], v[54:55], v[70:71] op_sel_hi:[1,0,1]
	v_pk_fma_f32 v[74:75], v[50:51], v[54:55], v[74:75] op_sel:[0,1,0]
	v_add_f32_dpp v182, v182, v182 row_ror:1 row_mask:0xf bank_mask:0xf bound_ctrl:1
	v_add_f32_dpp v183, v183, v183 row_ror:1 row_mask:0xf bank_mask:0xf bound_ctrl:1
	ds_read_b128 v[162:165], v80 offset:2048
	ds_read_b128 v[166:169], v80 offset:2304
	ds_read_b128 v[170:173], v80 offset:2560
	ds_read_b128 v[174:177], v80 offset:2816
	ds_write_b64 v2, v[182:183] offset:0
	v_pk_fma_f32 v[72:73], v[48:49], v[182:183], v[72:73] op_sel_hi:[1,0,1]
	v_pk_fma_f32 v[76:77], v[48:49], v[182:183], v[76:77] op_sel:[0,1,0]
	v_pk_fma_f32 v[70:71], v[46:47], v[182:183], v[70:71] op_sel_hi:[1,0,1]
	v_pk_fma_f32 v[74:75], v[46:47], v[182:183], v[74:75] op_sel:[0,1,0]
	s_waitcnt lgkmcnt(6)
	ds_read_b64 v[54:55], v81 offset:384
	v_pk_mul_f32 v[178:179], v[72:73], v[58:59]
	v_pk_mul_f32 v[180:181], v[76:77], v[58:59]
	v_pk_fma_f32 v[178:179], v[70:71], v[56:57], v[178:179]
	v_pk_fma_f32 v[180:181], v[74:75], v[56:57], v[180:181]
	v_add_f32_e32 v184, v178, v179
	v_add_f32_e32 v185, v180, v181
	v_pk_mul_f32 v[72:73], v[72:73], v[152:153]
	v_pk_mul_f32 v[76:77], v[76:77], v[152:153]
	v_add_f32_dpp v184, v184, v184 row_ror:8 row_mask:0xf bank_mask:0xf bound_ctrl:1
	v_add_f32_dpp v185, v185, v185 row_ror:8 row_mask:0xf bank_mask:0xf bound_ctrl:1
	v_pk_mul_f32 v[70:71], v[70:71], v[150:151]
	v_pk_mul_f32 v[74:75], v[74:75], v[150:151]
	v_add_f32_dpp v184, v184, v184 row_ror:4 row_mask:0xf bank_mask:0xf bound_ctrl:1
	v_add_f32_dpp v185, v185, v185 row_ror:4 row_mask:0xf bank_mask:0xf bound_ctrl:1
	v_pk_fma_f32 v[72:73], v[160:161], v[60:61], v[72:73] op_sel_hi:[1,0,1]
	v_pk_fma_f32 v[76:77], v[160:161], v[60:61], v[76:77] op_sel:[0,1,0]
	v_add_f32_dpp v184, v184, v184 row_ror:2 row_mask:0xf bank_mask:0xf bound_ctrl:1
	v_add_f32_dpp v185, v185, v185 row_ror:2 row_mask:0xf bank_mask:0xf bound_ctrl:1
	v_pk_fma_f32 v[70:71], v[158:159], v[60:61], v[70:71] op_sel_hi:[1,0,1]
	v_pk_fma_f32 v[74:75], v[158:159], v[60:61], v[74:75] op_sel:[0,1,0]
	v_add_f32_dpp v184, v184, v184 row_ror:1 row_mask:0xf bank_mask:0xf bound_ctrl:1
	v_add_f32_dpp v185, v185, v185 row_ror:1 row_mask:0xf bank_mask:0xf bound_ctrl:1
	ds_read_b128 v[38:41], v80 offset:3072
	ds_read_b128 v[42:45], v80 offset:3328
	ds_read_b128 v[46:49], v80 offset:3584
	ds_read_b128 v[50:53], v80 offset:3840
	ds_write_b64 v2, v[184:185] offset:128
	v_pk_fma_f32 v[72:73], v[156:157], v[184:185], v[72:73] op_sel_hi:[1,0,1]
	v_pk_fma_f32 v[76:77], v[156:157], v[184:185], v[76:77] op_sel:[0,1,0]
	v_pk_fma_f32 v[70:71], v[154:155], v[184:185], v[70:71] op_sel_hi:[1,0,1]
	v_pk_fma_f32 v[74:75], v[154:155], v[184:185], v[74:75] op_sel:[0,1,0]
	s_waitcnt lgkmcnt(7)
	ds_read_b64 v[60:61], v81 offset:512
	v_pk_mul_f32 v[178:179], v[72:73], v[164:165]
	v_pk_mul_f32 v[180:181], v[76:77], v[164:165]
	v_pk_fma_f32 v[178:179], v[70:71], v[162:163], v[178:179]
	v_pk_fma_f32 v[180:181], v[74:75], v[162:163], v[180:181]
	v_add_f32_e32 v182, v178, v179
	v_add_f32_e32 v183, v180, v181
	v_pk_mul_f32 v[72:73], v[72:73], v[168:169]
	v_pk_mul_f32 v[76:77], v[76:77], v[168:169]
	v_add_f32_dpp v182, v182, v182 row_ror:8 row_mask:0xf bank_mask:0xf bound_ctrl:1
	v_add_f32_dpp v183, v183, v183 row_ror:8 row_mask:0xf bank_mask:0xf bound_ctrl:1
	v_pk_mul_f32 v[70:71], v[70:71], v[166:167]
	v_pk_mul_f32 v[74:75], v[74:75], v[166:167]
	v_add_f32_dpp v182, v182, v182 row_ror:4 row_mask:0xf bank_mask:0xf bound_ctrl:1
	v_add_f32_dpp v183, v183, v183 row_ror:4 row_mask:0xf bank_mask:0xf bound_ctrl:1
	v_pk_fma_f32 v[72:73], v[176:177], v[78:79], v[72:73] op_sel_hi:[1,0,1]
	v_pk_fma_f32 v[76:77], v[176:177], v[78:79], v[76:77] op_sel:[0,1,0]
	v_add_f32_dpp v182, v182, v182 row_ror:2 row_mask:0xf bank_mask:0xf bound_ctrl:1
	v_add_f32_dpp v183, v183, v183 row_ror:2 row_mask:0xf bank_mask:0xf bound_ctrl:1
	v_pk_fma_f32 v[70:71], v[174:175], v[78:79], v[70:71] op_sel_hi:[1,0,1]
	v_pk_fma_f32 v[74:75], v[174:175], v[78:79], v[74:75] op_sel:[0,1,0]
	v_add_f32_dpp v182, v182, v182 row_ror:1 row_mask:0xf bank_mask:0xf bound_ctrl:1
	v_add_f32_dpp v183, v183, v183 row_ror:1 row_mask:0xf bank_mask:0xf bound_ctrl:1
	ds_read_b128 v[56:59], v80 offset:4096
	ds_read_b128 v[150:153], v80 offset:4352
	ds_read_b128 v[154:157], v80 offset:4608
	ds_read_b128 v[158:161], v80 offset:4864
	ds_write_b64 v2, v[182:183] offset:256
	v_pk_fma_f32 v[72:73], v[172:173], v[182:183], v[72:73] op_sel_hi:[1,0,1]
	v_pk_fma_f32 v[76:77], v[172:173], v[182:183], v[76:77] op_sel:[0,1,0]
	v_pk_fma_f32 v[70:71], v[170:171], v[182:183], v[70:71] op_sel_hi:[1,0,1]
	v_pk_fma_f32 v[74:75], v[170:171], v[182:183], v[74:75] op_sel:[0,1,0]
	s_waitcnt lgkmcnt(7)
	ds_read_b64 v[78:79], v81 offset:640
	v_pk_mul_f32 v[178:179], v[72:73], v[40:41]
	v_pk_mul_f32 v[180:181], v[76:77], v[40:41]
	v_pk_fma_f32 v[178:179], v[70:71], v[38:39], v[178:179]
	v_pk_fma_f32 v[180:181], v[74:75], v[38:39], v[180:181]
	v_add_f32_e32 v184, v178, v179
	v_add_f32_e32 v185, v180, v181
	v_pk_mul_f32 v[72:73], v[72:73], v[44:45]
	v_pk_mul_f32 v[76:77], v[76:77], v[44:45]
	v_add_f32_dpp v184, v184, v184 row_ror:8 row_mask:0xf bank_mask:0xf bound_ctrl:1
	v_add_f32_dpp v185, v185, v185 row_ror:8 row_mask:0xf bank_mask:0xf bound_ctrl:1
	v_pk_mul_f32 v[70:71], v[70:71], v[42:43]
	v_pk_mul_f32 v[74:75], v[74:75], v[42:43]
	v_add_f32_dpp v184, v184, v184 row_ror:4 row_mask:0xf bank_mask:0xf bound_ctrl:1
	v_add_f32_dpp v185, v185, v185 row_ror:4 row_mask:0xf bank_mask:0xf bound_ctrl:1
	v_pk_fma_f32 v[72:73], v[52:53], v[54:55], v[72:73] op_sel_hi:[1,0,1]
	v_pk_fma_f32 v[76:77], v[52:53], v[54:55], v[76:77] op_sel:[0,1,0]
	v_add_f32_dpp v184, v184, v184 row_ror:2 row_mask:0xf bank_mask:0xf bound_ctrl:1
	v_add_f32_dpp v185, v185, v185 row_ror:2 row_mask:0xf bank_mask:0xf bound_ctrl:1
	v_pk_fma_f32 v[70:71], v[50:51], v[54:55], v[70:71] op_sel_hi:[1,0,1]
	v_pk_fma_f32 v[74:75], v[50:51], v[54:55], v[74:75] op_sel:[0,1,0]
	v_add_f32_dpp v184, v184, v184 row_ror:1 row_mask:0xf bank_mask:0xf bound_ctrl:1
	v_add_f32_dpp v185, v185, v185 row_ror:1 row_mask:0xf bank_mask:0xf bound_ctrl:1
	ds_read_b128 v[162:165], v80 offset:5120
	ds_read_b128 v[166:169], v80 offset:5376
	ds_read_b128 v[170:173], v80 offset:5632
	ds_read_b128 v[174:177], v80 offset:5888
	ds_write_b64 v2, v[184:185] offset:384
	v_pk_fma_f32 v[72:73], v[48:49], v[184:185], v[72:73] op_sel_hi:[1,0,1]
	v_pk_fma_f32 v[76:77], v[48:49], v[184:185], v[76:77] op_sel:[0,1,0]
	v_pk_fma_f32 v[70:71], v[46:47], v[184:185], v[70:71] op_sel_hi:[1,0,1]
	v_pk_fma_f32 v[74:75], v[46:47], v[184:185], v[74:75] op_sel:[0,1,0]
	s_waitcnt lgkmcnt(7)
	ds_read_b64 v[54:55], v81 offset:768
	v_pk_mul_f32 v[178:179], v[72:73], v[58:59]
	v_pk_mul_f32 v[180:181], v[76:77], v[58:59]
	v_pk_fma_f32 v[178:179], v[70:71], v[56:57], v[178:179]
	v_pk_fma_f32 v[180:181], v[74:75], v[56:57], v[180:181]
	v_add_f32_e32 v182, v178, v179
	v_add_f32_e32 v183, v180, v181
	v_pk_mul_f32 v[72:73], v[72:73], v[152:153]
	v_pk_mul_f32 v[76:77], v[76:77], v[152:153]
	v_add_f32_dpp v182, v182, v182 row_ror:8 row_mask:0xf bank_mask:0xf bound_ctrl:1
	v_add_f32_dpp v183, v183, v183 row_ror:8 row_mask:0xf bank_mask:0xf bound_ctrl:1
	v_pk_mul_f32 v[70:71], v[70:71], v[150:151]
	v_pk_mul_f32 v[74:75], v[74:75], v[150:151]
	v_add_f32_dpp v182, v182, v182 row_ror:4 row_mask:0xf bank_mask:0xf bound_ctrl:1
	v_add_f32_dpp v183, v183, v183 row_ror:4 row_mask:0xf bank_mask:0xf bound_ctrl:1
	v_pk_fma_f32 v[72:73], v[160:161], v[60:61], v[72:73] op_sel_hi:[1,0,1]
	v_pk_fma_f32 v[76:77], v[160:161], v[60:61], v[76:77] op_sel:[0,1,0]
	v_add_f32_dpp v182, v182, v182 row_ror:2 row_mask:0xf bank_mask:0xf bound_ctrl:1
	v_add_f32_dpp v183, v183, v183 row_ror:2 row_mask:0xf bank_mask:0xf bound_ctrl:1
	v_pk_fma_f32 v[70:71], v[158:159], v[60:61], v[70:71] op_sel_hi:[1,0,1]
	v_pk_fma_f32 v[74:75], v[158:159], v[60:61], v[74:75] op_sel:[0,1,0]
	v_add_f32_dpp v182, v182, v182 row_ror:1 row_mask:0xf bank_mask:0xf bound_ctrl:1
	v_add_f32_dpp v183, v183, v183 row_ror:1 row_mask:0xf bank_mask:0xf bound_ctrl:1
	ds_read_b128 v[38:41], v80 offset:6144
	ds_read_b128 v[42:45], v80 offset:6400
	ds_read_b128 v[46:49], v80 offset:6656
	ds_read_b128 v[50:53], v80 offset:6912
	ds_write_b64 v2, v[182:183] offset:512
	v_pk_fma_f32 v[72:73], v[156:157], v[182:183], v[72:73] op_sel_hi:[1,0,1]
	v_pk_fma_f32 v[76:77], v[156:157], v[182:183], v[76:77] op_sel:[0,1,0]
	v_pk_fma_f32 v[70:71], v[154:155], v[182:183], v[70:71] op_sel_hi:[1,0,1]
	v_pk_fma_f32 v[74:75], v[154:155], v[182:183], v[74:75] op_sel:[0,1,0]
	s_waitcnt lgkmcnt(7)
	ds_read_b64 v[60:61], v81 offset:896
	v_pk_mul_f32 v[178:179], v[72:73], v[164:165]
	v_pk_mul_f32 v[180:181], v[76:77], v[164:165]
	v_pk_fma_f32 v[178:179], v[70:71], v[162:163], v[178:179]
	v_pk_fma_f32 v[180:181], v[74:75], v[162:163], v[180:181]
	v_add_f32_e32 v184, v178, v179
	v_add_f32_e32 v185, v180, v181
	v_pk_mul_f32 v[72:73], v[72:73], v[168:169]
	v_pk_mul_f32 v[76:77], v[76:77], v[168:169]
	v_add_f32_dpp v184, v184, v184 row_ror:8 row_mask:0xf bank_mask:0xf bound_ctrl:1
	v_add_f32_dpp v185, v185, v185 row_ror:8 row_mask:0xf bank_mask:0xf bound_ctrl:1
	v_pk_mul_f32 v[70:71], v[70:71], v[166:167]
	v_pk_mul_f32 v[74:75], v[74:75], v[166:167]
	v_add_f32_dpp v184, v184, v184 row_ror:4 row_mask:0xf bank_mask:0xf bound_ctrl:1
	v_add_f32_dpp v185, v185, v185 row_ror:4 row_mask:0xf bank_mask:0xf bound_ctrl:1
	v_pk_fma_f32 v[72:73], v[176:177], v[78:79], v[72:73] op_sel_hi:[1,0,1]
	v_pk_fma_f32 v[76:77], v[176:177], v[78:79], v[76:77] op_sel:[0,1,0]
	v_add_f32_dpp v184, v184, v184 row_ror:2 row_mask:0xf bank_mask:0xf bound_ctrl:1
	v_add_f32_dpp v185, v185, v185 row_ror:2 row_mask:0xf bank_mask:0xf bound_ctrl:1
	v_pk_fma_f32 v[70:71], v[174:175], v[78:79], v[70:71] op_sel_hi:[1,0,1]
	v_pk_fma_f32 v[74:75], v[174:175], v[78:79], v[74:75] op_sel:[0,1,0]
	v_add_f32_dpp v184, v184, v184 row_ror:1 row_mask:0xf bank_mask:0xf bound_ctrl:1
	v_add_f32_dpp v185, v185, v185 row_ror:1 row_mask:0xf bank_mask:0xf bound_ctrl:1
	ds_read_b128 v[56:59], v80 offset:7168
	ds_read_b128 v[150:153], v80 offset:7424
	ds_read_b128 v[154:157], v80 offset:7680
	ds_read_b128 v[158:161], v80 offset:7936
	ds_write_b64 v2, v[184:185] offset:640
	v_pk_fma_f32 v[72:73], v[172:173], v[184:185], v[72:73] op_sel_hi:[1,0,1]
	v_pk_fma_f32 v[76:77], v[172:173], v[184:185], v[76:77] op_sel:[0,1,0]
	v_pk_fma_f32 v[70:71], v[170:171], v[184:185], v[70:71] op_sel_hi:[1,0,1]
	v_pk_fma_f32 v[74:75], v[170:171], v[184:185], v[74:75] op_sel:[0,1,0]
	s_waitcnt lgkmcnt(7)
	ds_read_b64 v[78:79], v81 offset:1024
	v_pk_mul_f32 v[178:179], v[72:73], v[40:41]
	v_pk_mul_f32 v[180:181], v[76:77], v[40:41]
	v_pk_fma_f32 v[178:179], v[70:71], v[38:39], v[178:179]
	v_pk_fma_f32 v[180:181], v[74:75], v[38:39], v[180:181]
	v_add_f32_e32 v182, v178, v179
	v_add_f32_e32 v183, v180, v181
	v_pk_mul_f32 v[72:73], v[72:73], v[44:45]
	v_pk_mul_f32 v[76:77], v[76:77], v[44:45]
	v_add_f32_dpp v182, v182, v182 row_ror:8 row_mask:0xf bank_mask:0xf bound_ctrl:1
	v_add_f32_dpp v183, v183, v183 row_ror:8 row_mask:0xf bank_mask:0xf bound_ctrl:1
	v_pk_mul_f32 v[70:71], v[70:71], v[42:43]
	v_pk_mul_f32 v[74:75], v[74:75], v[42:43]
	v_add_f32_dpp v182, v182, v182 row_ror:4 row_mask:0xf bank_mask:0xf bound_ctrl:1
	v_add_f32_dpp v183, v183, v183 row_ror:4 row_mask:0xf bank_mask:0xf bound_ctrl:1
	v_pk_fma_f32 v[72:73], v[52:53], v[54:55], v[72:73] op_sel_hi:[1,0,1]
	v_pk_fma_f32 v[76:77], v[52:53], v[54:55], v[76:77] op_sel:[0,1,0]
	v_add_f32_dpp v182, v182, v182 row_ror:2 row_mask:0xf bank_mask:0xf bound_ctrl:1
	v_add_f32_dpp v183, v183, v183 row_ror:2 row_mask:0xf bank_mask:0xf bound_ctrl:1
	v_pk_fma_f32 v[70:71], v[50:51], v[54:55], v[70:71] op_sel_hi:[1,0,1]
	v_pk_fma_f32 v[74:75], v[50:51], v[54:55], v[74:75] op_sel:[0,1,0]
	v_add_f32_dpp v182, v182, v182 row_ror:1 row_mask:0xf bank_mask:0xf bound_ctrl:1
	v_add_f32_dpp v183, v183, v183 row_ror:1 row_mask:0xf bank_mask:0xf bound_ctrl:1
	ds_read_b128 v[162:165], v80 offset:8192
	ds_read_b128 v[166:169], v80 offset:8448
	ds_read_b128 v[170:173], v80 offset:8704
	ds_read_b128 v[174:177], v80 offset:8960
	ds_write_b64 v2, v[182:183] offset:768
	v_pk_fma_f32 v[72:73], v[48:49], v[182:183], v[72:73] op_sel_hi:[1,0,1]
	v_pk_fma_f32 v[76:77], v[48:49], v[182:183], v[76:77] op_sel:[0,1,0]
	v_pk_fma_f32 v[70:71], v[46:47], v[182:183], v[70:71] op_sel_hi:[1,0,1]
	v_pk_fma_f32 v[74:75], v[46:47], v[182:183], v[74:75] op_sel:[0,1,0]
	s_waitcnt lgkmcnt(7)
	ds_read_b64 v[54:55], v81 offset:1152
	v_pk_mul_f32 v[178:179], v[72:73], v[58:59]
	v_pk_mul_f32 v[180:181], v[76:77], v[58:59]
	v_pk_fma_f32 v[178:179], v[70:71], v[56:57], v[178:179]
	v_pk_fma_f32 v[180:181], v[74:75], v[56:57], v[180:181]
	v_add_f32_e32 v184, v178, v179
	v_add_f32_e32 v185, v180, v181
	v_pk_mul_f32 v[72:73], v[72:73], v[152:153]
	v_pk_mul_f32 v[76:77], v[76:77], v[152:153]
	v_add_f32_dpp v184, v184, v184 row_ror:8 row_mask:0xf bank_mask:0xf bound_ctrl:1
	v_add_f32_dpp v185, v185, v185 row_ror:8 row_mask:0xf bank_mask:0xf bound_ctrl:1
	v_pk_mul_f32 v[70:71], v[70:71], v[150:151]
	v_pk_mul_f32 v[74:75], v[74:75], v[150:151]
	v_add_f32_dpp v184, v184, v184 row_ror:4 row_mask:0xf bank_mask:0xf bound_ctrl:1
	v_add_f32_dpp v185, v185, v185 row_ror:4 row_mask:0xf bank_mask:0xf bound_ctrl:1
	v_pk_fma_f32 v[72:73], v[160:161], v[60:61], v[72:73] op_sel_hi:[1,0,1]
	v_pk_fma_f32 v[76:77], v[160:161], v[60:61], v[76:77] op_sel:[0,1,0]
	v_add_f32_dpp v184, v184, v184 row_ror:2 row_mask:0xf bank_mask:0xf bound_ctrl:1
	v_add_f32_dpp v185, v185, v185 row_ror:2 row_mask:0xf bank_mask:0xf bound_ctrl:1
	v_pk_fma_f32 v[70:71], v[158:159], v[60:61], v[70:71] op_sel_hi:[1,0,1]
	v_pk_fma_f32 v[74:75], v[158:159], v[60:61], v[74:75] op_sel:[0,1,0]
	v_add_f32_dpp v184, v184, v184 row_ror:1 row_mask:0xf bank_mask:0xf bound_ctrl:1
	v_add_f32_dpp v185, v185, v185 row_ror:1 row_mask:0xf bank_mask:0xf bound_ctrl:1
	ds_read_b128 v[38:41], v80 offset:9216
	ds_read_b128 v[42:45], v80 offset:9472
	ds_read_b128 v[46:49], v80 offset:9728
	ds_read_b128 v[50:53], v80 offset:9984
	ds_write_b64 v2, v[184:185] offset:896
	v_pk_fma_f32 v[72:73], v[156:157], v[184:185], v[72:73] op_sel_hi:[1,0,1]
	v_pk_fma_f32 v[76:77], v[156:157], v[184:185], v[76:77] op_sel:[0,1,0]
	v_pk_fma_f32 v[70:71], v[154:155], v[184:185], v[70:71] op_sel_hi:[1,0,1]
	v_pk_fma_f32 v[74:75], v[154:155], v[184:185], v[74:75] op_sel:[0,1,0]
	s_waitcnt lgkmcnt(7)
	ds_read_b64 v[60:61], v81 offset:1280
	v_pk_mul_f32 v[178:179], v[72:73], v[164:165]
	v_pk_mul_f32 v[180:181], v[76:77], v[164:165]
	v_pk_fma_f32 v[178:179], v[70:71], v[162:163], v[178:179]
	v_pk_fma_f32 v[180:181], v[74:75], v[162:163], v[180:181]
	v_add_f32_e32 v182, v178, v179
	v_add_f32_e32 v183, v180, v181
	v_pk_mul_f32 v[72:73], v[72:73], v[168:169]
	v_pk_mul_f32 v[76:77], v[76:77], v[168:169]
	v_add_f32_dpp v182, v182, v182 row_ror:8 row_mask:0xf bank_mask:0xf bound_ctrl:1
	v_add_f32_dpp v183, v183, v183 row_ror:8 row_mask:0xf bank_mask:0xf bound_ctrl:1
	v_pk_mul_f32 v[70:71], v[70:71], v[166:167]
	v_pk_mul_f32 v[74:75], v[74:75], v[166:167]
	v_add_f32_dpp v182, v182, v182 row_ror:4 row_mask:0xf bank_mask:0xf bound_ctrl:1
	v_add_f32_dpp v183, v183, v183 row_ror:4 row_mask:0xf bank_mask:0xf bound_ctrl:1
	v_pk_fma_f32 v[72:73], v[176:177], v[78:79], v[72:73] op_sel_hi:[1,0,1]
	v_pk_fma_f32 v[76:77], v[176:177], v[78:79], v[76:77] op_sel:[0,1,0]
	v_add_f32_dpp v182, v182, v182 row_ror:2 row_mask:0xf bank_mask:0xf bound_ctrl:1
	v_add_f32_dpp v183, v183, v183 row_ror:2 row_mask:0xf bank_mask:0xf bound_ctrl:1
	v_pk_fma_f32 v[70:71], v[174:175], v[78:79], v[70:71] op_sel_hi:[1,0,1]
	v_pk_fma_f32 v[74:75], v[174:175], v[78:79], v[74:75] op_sel:[0,1,0]
	v_add_f32_dpp v182, v182, v182 row_ror:1 row_mask:0xf bank_mask:0xf bound_ctrl:1
	v_add_f32_dpp v183, v183, v183 row_ror:1 row_mask:0xf bank_mask:0xf bound_ctrl:1
	ds_read_b128 v[56:59], v80 offset:10240
	ds_read_b128 v[150:153], v80 offset:10496
	ds_read_b128 v[154:157], v80 offset:10752
	ds_read_b128 v[158:161], v80 offset:11008
	ds_write_b64 v2, v[182:183] offset:1024
	v_pk_fma_f32 v[72:73], v[172:173], v[182:183], v[72:73] op_sel_hi:[1,0,1]
	v_pk_fma_f32 v[76:77], v[172:173], v[182:183], v[76:77] op_sel:[0,1,0]
	v_pk_fma_f32 v[70:71], v[170:171], v[182:183], v[70:71] op_sel_hi:[1,0,1]
	v_pk_fma_f32 v[74:75], v[170:171], v[182:183], v[74:75] op_sel:[0,1,0]
	s_waitcnt lgkmcnt(7)
	ds_read_b64 v[78:79], v81 offset:1408
	v_pk_mul_f32 v[178:179], v[72:73], v[40:41]
	v_pk_mul_f32 v[180:181], v[76:77], v[40:41]
	v_pk_fma_f32 v[178:179], v[70:71], v[38:39], v[178:179]
	v_pk_fma_f32 v[180:181], v[74:75], v[38:39], v[180:181]
	v_add_f32_e32 v184, v178, v179
	v_add_f32_e32 v185, v180, v181
	v_pk_mul_f32 v[72:73], v[72:73], v[44:45]
	v_pk_mul_f32 v[76:77], v[76:77], v[44:45]
	v_add_f32_dpp v184, v184, v184 row_ror:8 row_mask:0xf bank_mask:0xf bound_ctrl:1
	v_add_f32_dpp v185, v185, v185 row_ror:8 row_mask:0xf bank_mask:0xf bound_ctrl:1
	v_pk_mul_f32 v[70:71], v[70:71], v[42:43]
	v_pk_mul_f32 v[74:75], v[74:75], v[42:43]
	v_add_f32_dpp v184, v184, v184 row_ror:4 row_mask:0xf bank_mask:0xf bound_ctrl:1
	v_add_f32_dpp v185, v185, v185 row_ror:4 row_mask:0xf bank_mask:0xf bound_ctrl:1
	v_pk_fma_f32 v[72:73], v[52:53], v[54:55], v[72:73] op_sel_hi:[1,0,1]
	v_pk_fma_f32 v[76:77], v[52:53], v[54:55], v[76:77] op_sel:[0,1,0]
	v_add_f32_dpp v184, v184, v184 row_ror:2 row_mask:0xf bank_mask:0xf bound_ctrl:1
	v_add_f32_dpp v185, v185, v185 row_ror:2 row_mask:0xf bank_mask:0xf bound_ctrl:1
	v_pk_fma_f32 v[70:71], v[50:51], v[54:55], v[70:71] op_sel_hi:[1,0,1]
	v_pk_fma_f32 v[74:75], v[50:51], v[54:55], v[74:75] op_sel:[0,1,0]
	v_add_f32_dpp v184, v184, v184 row_ror:1 row_mask:0xf bank_mask:0xf bound_ctrl:1
	v_add_f32_dpp v185, v185, v185 row_ror:1 row_mask:0xf bank_mask:0xf bound_ctrl:1
	ds_read_b128 v[162:165], v80 offset:11264
	ds_read_b128 v[166:169], v80 offset:11520
	ds_read_b128 v[170:173], v80 offset:11776
	ds_read_b128 v[174:177], v80 offset:12032
	ds_write_b64 v2, v[184:185] offset:1152
	v_pk_fma_f32 v[72:73], v[48:49], v[184:185], v[72:73] op_sel_hi:[1,0,1]
	v_pk_fma_f32 v[76:77], v[48:49], v[184:185], v[76:77] op_sel:[0,1,0]
	v_pk_fma_f32 v[70:71], v[46:47], v[184:185], v[70:71] op_sel_hi:[1,0,1]
	v_pk_fma_f32 v[74:75], v[46:47], v[184:185], v[74:75] op_sel:[0,1,0]
	s_waitcnt lgkmcnt(7)
	ds_read_b64 v[54:55], v81 offset:1536
	v_pk_mul_f32 v[178:179], v[72:73], v[58:59]
	v_pk_mul_f32 v[180:181], v[76:77], v[58:59]
	v_pk_fma_f32 v[178:179], v[70:71], v[56:57], v[178:179]
	v_pk_fma_f32 v[180:181], v[74:75], v[56:57], v[180:181]
	v_add_f32_e32 v182, v178, v179
	v_add_f32_e32 v183, v180, v181
	v_pk_mul_f32 v[72:73], v[72:73], v[152:153]
	v_pk_mul_f32 v[76:77], v[76:77], v[152:153]
	v_add_f32_dpp v182, v182, v182 row_ror:8 row_mask:0xf bank_mask:0xf bound_ctrl:1
	v_add_f32_dpp v183, v183, v183 row_ror:8 row_mask:0xf bank_mask:0xf bound_ctrl:1
	v_pk_mul_f32 v[70:71], v[70:71], v[150:151]
	v_pk_mul_f32 v[74:75], v[74:75], v[150:151]
	v_add_f32_dpp v182, v182, v182 row_ror:4 row_mask:0xf bank_mask:0xf bound_ctrl:1
	v_add_f32_dpp v183, v183, v183 row_ror:4 row_mask:0xf bank_mask:0xf bound_ctrl:1
	v_pk_fma_f32 v[72:73], v[160:161], v[60:61], v[72:73] op_sel_hi:[1,0,1]
	v_pk_fma_f32 v[76:77], v[160:161], v[60:61], v[76:77] op_sel:[0,1,0]
	v_add_f32_dpp v182, v182, v182 row_ror:2 row_mask:0xf bank_mask:0xf bound_ctrl:1
	v_add_f32_dpp v183, v183, v183 row_ror:2 row_mask:0xf bank_mask:0xf bound_ctrl:1
	v_pk_fma_f32 v[70:71], v[158:159], v[60:61], v[70:71] op_sel_hi:[1,0,1]
	v_pk_fma_f32 v[74:75], v[158:159], v[60:61], v[74:75] op_sel:[0,1,0]
	v_add_f32_dpp v182, v182, v182 row_ror:1 row_mask:0xf bank_mask:0xf bound_ctrl:1
	v_add_f32_dpp v183, v183, v183 row_ror:1 row_mask:0xf bank_mask:0xf bound_ctrl:1
	ds_read_b128 v[38:41], v80 offset:12288
	ds_read_b128 v[42:45], v80 offset:12544
	ds_read_b128 v[46:49], v80 offset:12800
	ds_read_b128 v[50:53], v80 offset:13056
	ds_write_b64 v2, v[182:183] offset:1280
	v_pk_fma_f32 v[72:73], v[156:157], v[182:183], v[72:73] op_sel_hi:[1,0,1]
	v_pk_fma_f32 v[76:77], v[156:157], v[182:183], v[76:77] op_sel:[0,1,0]
	v_pk_fma_f32 v[70:71], v[154:155], v[182:183], v[70:71] op_sel_hi:[1,0,1]
	v_pk_fma_f32 v[74:75], v[154:155], v[182:183], v[74:75] op_sel:[0,1,0]
	s_waitcnt lgkmcnt(7)
	ds_read_b64 v[60:61], v81 offset:1664
	v_pk_mul_f32 v[178:179], v[72:73], v[164:165]
	v_pk_mul_f32 v[180:181], v[76:77], v[164:165]
	v_pk_fma_f32 v[178:179], v[70:71], v[162:163], v[178:179]
	v_pk_fma_f32 v[180:181], v[74:75], v[162:163], v[180:181]
	v_add_f32_e32 v184, v178, v179
	v_add_f32_e32 v185, v180, v181
	v_pk_mul_f32 v[72:73], v[72:73], v[168:169]
	v_pk_mul_f32 v[76:77], v[76:77], v[168:169]
	v_add_f32_dpp v184, v184, v184 row_ror:8 row_mask:0xf bank_mask:0xf bound_ctrl:1
	v_add_f32_dpp v185, v185, v185 row_ror:8 row_mask:0xf bank_mask:0xf bound_ctrl:1
	v_pk_mul_f32 v[70:71], v[70:71], v[166:167]
	v_pk_mul_f32 v[74:75], v[74:75], v[166:167]
	v_add_f32_dpp v184, v184, v184 row_ror:4 row_mask:0xf bank_mask:0xf bound_ctrl:1
	v_add_f32_dpp v185, v185, v185 row_ror:4 row_mask:0xf bank_mask:0xf bound_ctrl:1
	v_pk_fma_f32 v[72:73], v[176:177], v[78:79], v[72:73] op_sel_hi:[1,0,1]
	v_pk_fma_f32 v[76:77], v[176:177], v[78:79], v[76:77] op_sel:[0,1,0]
	v_add_f32_dpp v184, v184, v184 row_ror:2 row_mask:0xf bank_mask:0xf bound_ctrl:1
	v_add_f32_dpp v185, v185, v185 row_ror:2 row_mask:0xf bank_mask:0xf bound_ctrl:1
	v_pk_fma_f32 v[70:71], v[174:175], v[78:79], v[70:71] op_sel_hi:[1,0,1]
	v_pk_fma_f32 v[74:75], v[174:175], v[78:79], v[74:75] op_sel:[0,1,0]
	v_add_f32_dpp v184, v184, v184 row_ror:1 row_mask:0xf bank_mask:0xf bound_ctrl:1
	v_add_f32_dpp v185, v185, v185 row_ror:1 row_mask:0xf bank_mask:0xf bound_ctrl:1
	ds_read_b128 v[56:59], v80 offset:13312
	ds_read_b128 v[150:153], v80 offset:13568
	ds_read_b128 v[154:157], v80 offset:13824
	ds_read_b128 v[158:161], v80 offset:14080
	ds_write_b64 v2, v[184:185] offset:1408
	v_pk_fma_f32 v[72:73], v[172:173], v[184:185], v[72:73] op_sel_hi:[1,0,1]
	v_pk_fma_f32 v[76:77], v[172:173], v[184:185], v[76:77] op_sel:[0,1,0]
	v_pk_fma_f32 v[70:71], v[170:171], v[184:185], v[70:71] op_sel_hi:[1,0,1]
	v_pk_fma_f32 v[74:75], v[170:171], v[184:185], v[74:75] op_sel:[0,1,0]
	s_waitcnt lgkmcnt(7)
	ds_read_b64 v[78:79], v81 offset:1792
	v_pk_mul_f32 v[178:179], v[72:73], v[40:41]
	v_pk_mul_f32 v[180:181], v[76:77], v[40:41]
	v_pk_fma_f32 v[178:179], v[70:71], v[38:39], v[178:179]
	v_pk_fma_f32 v[180:181], v[74:75], v[38:39], v[180:181]
	v_add_f32_e32 v182, v178, v179
	v_add_f32_e32 v183, v180, v181
	v_pk_mul_f32 v[72:73], v[72:73], v[44:45]
	v_pk_mul_f32 v[76:77], v[76:77], v[44:45]
	v_add_f32_dpp v182, v182, v182 row_ror:8 row_mask:0xf bank_mask:0xf bound_ctrl:1
	v_add_f32_dpp v183, v183, v183 row_ror:8 row_mask:0xf bank_mask:0xf bound_ctrl:1
	v_pk_mul_f32 v[70:71], v[70:71], v[42:43]
	v_pk_mul_f32 v[74:75], v[74:75], v[42:43]
	v_add_f32_dpp v182, v182, v182 row_ror:4 row_mask:0xf bank_mask:0xf bound_ctrl:1
	v_add_f32_dpp v183, v183, v183 row_ror:4 row_mask:0xf bank_mask:0xf bound_ctrl:1
	v_pk_fma_f32 v[72:73], v[52:53], v[54:55], v[72:73] op_sel_hi:[1,0,1]
	v_pk_fma_f32 v[76:77], v[52:53], v[54:55], v[76:77] op_sel:[0,1,0]
	v_add_f32_dpp v182, v182, v182 row_ror:2 row_mask:0xf bank_mask:0xf bound_ctrl:1
	v_add_f32_dpp v183, v183, v183 row_ror:2 row_mask:0xf bank_mask:0xf bound_ctrl:1
	v_pk_fma_f32 v[70:71], v[50:51], v[54:55], v[70:71] op_sel_hi:[1,0,1]
	v_pk_fma_f32 v[74:75], v[50:51], v[54:55], v[74:75] op_sel:[0,1,0]
	v_add_f32_dpp v182, v182, v182 row_ror:1 row_mask:0xf bank_mask:0xf bound_ctrl:1
	v_add_f32_dpp v183, v183, v183 row_ror:1 row_mask:0xf bank_mask:0xf bound_ctrl:1
	ds_read_b128 v[162:165], v80 offset:14336
	ds_read_b128 v[166:169], v80 offset:14592
	ds_read_b128 v[170:173], v80 offset:14848
	ds_read_b128 v[174:177], v80 offset:15104
	ds_write_b64 v2, v[182:183] offset:1536
	v_pk_fma_f32 v[72:73], v[48:49], v[182:183], v[72:73] op_sel_hi:[1,0,1]
	v_pk_fma_f32 v[76:77], v[48:49], v[182:183], v[76:77] op_sel:[0,1,0]
	v_pk_fma_f32 v[70:71], v[46:47], v[182:183], v[70:71] op_sel_hi:[1,0,1]
	v_pk_fma_f32 v[74:75], v[46:47], v[182:183], v[74:75] op_sel:[0,1,0]
	s_waitcnt lgkmcnt(7)
	ds_read_b64 v[54:55], v81 offset:1920
	v_pk_mul_f32 v[178:179], v[72:73], v[58:59]
	v_pk_mul_f32 v[180:181], v[76:77], v[58:59]
	v_pk_fma_f32 v[178:179], v[70:71], v[56:57], v[178:179]
	v_pk_fma_f32 v[180:181], v[74:75], v[56:57], v[180:181]
	v_add_f32_e32 v184, v178, v179
	v_add_f32_e32 v185, v180, v181
	v_pk_mul_f32 v[72:73], v[72:73], v[152:153]
	v_pk_mul_f32 v[76:77], v[76:77], v[152:153]
	v_add_f32_dpp v184, v184, v184 row_ror:8 row_mask:0xf bank_mask:0xf bound_ctrl:1
	v_add_f32_dpp v185, v185, v185 row_ror:8 row_mask:0xf bank_mask:0xf bound_ctrl:1
	v_pk_mul_f32 v[70:71], v[70:71], v[150:151]
	v_pk_mul_f32 v[74:75], v[74:75], v[150:151]
	v_add_f32_dpp v184, v184, v184 row_ror:4 row_mask:0xf bank_mask:0xf bound_ctrl:1
	v_add_f32_dpp v185, v185, v185 row_ror:4 row_mask:0xf bank_mask:0xf bound_ctrl:1
	v_pk_fma_f32 v[72:73], v[160:161], v[60:61], v[72:73] op_sel_hi:[1,0,1]
	v_pk_fma_f32 v[76:77], v[160:161], v[60:61], v[76:77] op_sel:[0,1,0]
	v_add_f32_dpp v184, v184, v184 row_ror:2 row_mask:0xf bank_mask:0xf bound_ctrl:1
	v_add_f32_dpp v185, v185, v185 row_ror:2 row_mask:0xf bank_mask:0xf bound_ctrl:1
	v_pk_fma_f32 v[70:71], v[158:159], v[60:61], v[70:71] op_sel_hi:[1,0,1]
	v_pk_fma_f32 v[74:75], v[158:159], v[60:61], v[74:75] op_sel:[0,1,0]
	v_add_f32_dpp v184, v184, v184 row_ror:1 row_mask:0xf bank_mask:0xf bound_ctrl:1
	v_add_f32_dpp v185, v185, v185 row_ror:1 row_mask:0xf bank_mask:0xf bound_ctrl:1
	ds_read_b128 v[38:41], v80 offset:15360
	ds_read_b128 v[42:45], v80 offset:15616
	ds_read_b128 v[46:49], v80 offset:15872
	ds_read_b128 v[50:53], v80 offset:16128
	ds_write_b64 v2, v[184:185] offset:1664
	v_pk_fma_f32 v[72:73], v[156:157], v[184:185], v[72:73] op_sel_hi:[1,0,1]
	v_pk_fma_f32 v[76:77], v[156:157], v[184:185], v[76:77] op_sel:[0,1,0]
	v_pk_fma_f32 v[70:71], v[154:155], v[184:185], v[70:71] op_sel_hi:[1,0,1]
	v_pk_fma_f32 v[74:75], v[154:155], v[184:185], v[74:75] op_sel:[0,1,0]
	s_waitcnt lgkmcnt(7)
	ds_read_b64 v[60:61], v81 offset:2048
	v_pk_mul_f32 v[178:179], v[72:73], v[164:165]
	v_pk_mul_f32 v[180:181], v[76:77], v[164:165]
	v_pk_fma_f32 v[178:179], v[70:71], v[162:163], v[178:179]
	v_pk_fma_f32 v[180:181], v[74:75], v[162:163], v[180:181]
	v_add_f32_e32 v182, v178, v179
	v_add_f32_e32 v183, v180, v181
	v_pk_mul_f32 v[72:73], v[72:73], v[168:169]
	v_pk_mul_f32 v[76:77], v[76:77], v[168:169]
	v_add_f32_dpp v182, v182, v182 row_ror:8 row_mask:0xf bank_mask:0xf bound_ctrl:1
	v_add_f32_dpp v183, v183, v183 row_ror:8 row_mask:0xf bank_mask:0xf bound_ctrl:1
	v_pk_mul_f32 v[70:71], v[70:71], v[166:167]
	v_pk_mul_f32 v[74:75], v[74:75], v[166:167]
	v_add_f32_dpp v182, v182, v182 row_ror:4 row_mask:0xf bank_mask:0xf bound_ctrl:1
	v_add_f32_dpp v183, v183, v183 row_ror:4 row_mask:0xf bank_mask:0xf bound_ctrl:1
	v_pk_fma_f32 v[72:73], v[176:177], v[78:79], v[72:73] op_sel_hi:[1,0,1]
	v_pk_fma_f32 v[76:77], v[176:177], v[78:79], v[76:77] op_sel:[0,1,0]
	v_add_f32_dpp v182, v182, v182 row_ror:2 row_mask:0xf bank_mask:0xf bound_ctrl:1
	v_add_f32_dpp v183, v183, v183 row_ror:2 row_mask:0xf bank_mask:0xf bound_ctrl:1
	v_pk_fma_f32 v[70:71], v[174:175], v[78:79], v[70:71] op_sel_hi:[1,0,1]
	v_pk_fma_f32 v[74:75], v[174:175], v[78:79], v[74:75] op_sel:[0,1,0]
	v_add_f32_dpp v182, v182, v182 row_ror:1 row_mask:0xf bank_mask:0xf bound_ctrl:1
	v_add_f32_dpp v183, v183, v183 row_ror:1 row_mask:0xf bank_mask:0xf bound_ctrl:1
	ds_read_b128 v[56:59], v80 offset:16384
	ds_read_b128 v[150:153], v80 offset:16640
	ds_read_b128 v[154:157], v80 offset:16896
	ds_read_b128 v[158:161], v80 offset:17152
	ds_write_b64 v2, v[182:183] offset:1792
	v_pk_fma_f32 v[72:73], v[172:173], v[182:183], v[72:73] op_sel_hi:[1,0,1]
	v_pk_fma_f32 v[76:77], v[172:173], v[182:183], v[76:77] op_sel:[0,1,0]
	v_pk_fma_f32 v[70:71], v[170:171], v[182:183], v[70:71] op_sel_hi:[1,0,1]
	v_pk_fma_f32 v[74:75], v[170:171], v[182:183], v[74:75] op_sel:[0,1,0]
	s_waitcnt lgkmcnt(7)
	ds_read_b64 v[78:79], v81 offset:2176
	v_pk_mul_f32 v[178:179], v[72:73], v[40:41]
	v_pk_mul_f32 v[180:181], v[76:77], v[40:41]
	v_pk_fma_f32 v[178:179], v[70:71], v[38:39], v[178:179]
	v_pk_fma_f32 v[180:181], v[74:75], v[38:39], v[180:181]
	v_add_f32_e32 v184, v178, v179
	v_add_f32_e32 v185, v180, v181
	v_pk_mul_f32 v[72:73], v[72:73], v[44:45]
	v_pk_mul_f32 v[76:77], v[76:77], v[44:45]
	v_add_f32_dpp v184, v184, v184 row_ror:8 row_mask:0xf bank_mask:0xf bound_ctrl:1
	v_add_f32_dpp v185, v185, v185 row_ror:8 row_mask:0xf bank_mask:0xf bound_ctrl:1
	v_pk_mul_f32 v[70:71], v[70:71], v[42:43]
	v_pk_mul_f32 v[74:75], v[74:75], v[42:43]
	v_add_f32_dpp v184, v184, v184 row_ror:4 row_mask:0xf bank_mask:0xf bound_ctrl:1
	v_add_f32_dpp v185, v185, v185 row_ror:4 row_mask:0xf bank_mask:0xf bound_ctrl:1
	v_pk_fma_f32 v[72:73], v[52:53], v[54:55], v[72:73] op_sel_hi:[1,0,1]
	v_pk_fma_f32 v[76:77], v[52:53], v[54:55], v[76:77] op_sel:[0,1,0]
	v_add_f32_dpp v184, v184, v184 row_ror:2 row_mask:0xf bank_mask:0xf bound_ctrl:1
	v_add_f32_dpp v185, v185, v185 row_ror:2 row_mask:0xf bank_mask:0xf bound_ctrl:1
	v_pk_fma_f32 v[70:71], v[50:51], v[54:55], v[70:71] op_sel_hi:[1,0,1]
	v_pk_fma_f32 v[74:75], v[50:51], v[54:55], v[74:75] op_sel:[0,1,0]
	v_add_f32_dpp v184, v184, v184 row_ror:1 row_mask:0xf bank_mask:0xf bound_ctrl:1
	v_add_f32_dpp v185, v185, v185 row_ror:1 row_mask:0xf bank_mask:0xf bound_ctrl:1
	ds_read_b128 v[162:165], v80 offset:17408
	ds_read_b128 v[166:169], v80 offset:17664
	ds_read_b128 v[170:173], v80 offset:17920
	ds_read_b128 v[174:177], v80 offset:18176
	ds_write_b64 v2, v[184:185] offset:1920
	v_pk_fma_f32 v[72:73], v[48:49], v[184:185], v[72:73] op_sel_hi:[1,0,1]
	v_pk_fma_f32 v[76:77], v[48:49], v[184:185], v[76:77] op_sel:[0,1,0]
	v_pk_fma_f32 v[70:71], v[46:47], v[184:185], v[70:71] op_sel_hi:[1,0,1]
	v_pk_fma_f32 v[74:75], v[46:47], v[184:185], v[74:75] op_sel:[0,1,0]
	s_waitcnt lgkmcnt(7)
	ds_read_b64 v[54:55], v81 offset:2304
	v_pk_mul_f32 v[178:179], v[72:73], v[58:59]
	v_pk_mul_f32 v[180:181], v[76:77], v[58:59]
	v_pk_fma_f32 v[178:179], v[70:71], v[56:57], v[178:179]
	v_pk_fma_f32 v[180:181], v[74:75], v[56:57], v[180:181]
	v_add_f32_e32 v182, v178, v179
	v_add_f32_e32 v183, v180, v181
	v_pk_mul_f32 v[72:73], v[72:73], v[152:153]
	v_pk_mul_f32 v[76:77], v[76:77], v[152:153]
	v_add_f32_dpp v182, v182, v182 row_ror:8 row_mask:0xf bank_mask:0xf bound_ctrl:1
	v_add_f32_dpp v183, v183, v183 row_ror:8 row_mask:0xf bank_mask:0xf bound_ctrl:1
	v_pk_mul_f32 v[70:71], v[70:71], v[150:151]
	v_pk_mul_f32 v[74:75], v[74:75], v[150:151]
	v_add_f32_dpp v182, v182, v182 row_ror:4 row_mask:0xf bank_mask:0xf bound_ctrl:1
	v_add_f32_dpp v183, v183, v183 row_ror:4 row_mask:0xf bank_mask:0xf bound_ctrl:1
	v_pk_fma_f32 v[72:73], v[160:161], v[60:61], v[72:73] op_sel_hi:[1,0,1]
	v_pk_fma_f32 v[76:77], v[160:161], v[60:61], v[76:77] op_sel:[0,1,0]
	v_add_f32_dpp v182, v182, v182 row_ror:2 row_mask:0xf bank_mask:0xf bound_ctrl:1
	v_add_f32_dpp v183, v183, v183 row_ror:2 row_mask:0xf bank_mask:0xf bound_ctrl:1
	v_pk_fma_f32 v[70:71], v[158:159], v[60:61], v[70:71] op_sel_hi:[1,0,1]
	v_pk_fma_f32 v[74:75], v[158:159], v[60:61], v[74:75] op_sel:[0,1,0]
	v_add_f32_dpp v182, v182, v182 row_ror:1 row_mask:0xf bank_mask:0xf bound_ctrl:1
	v_add_f32_dpp v183, v183, v183 row_ror:1 row_mask:0xf bank_mask:0xf bound_ctrl:1
	ds_read_b128 v[38:41], v80 offset:18432
	ds_read_b128 v[42:45], v80 offset:18688
	ds_read_b128 v[46:49], v80 offset:18944
	ds_read_b128 v[50:53], v80 offset:19200
	ds_write_b64 v2, v[182:183] offset:2048
	v_pk_fma_f32 v[72:73], v[156:157], v[182:183], v[72:73] op_sel_hi:[1,0,1]
	v_pk_fma_f32 v[76:77], v[156:157], v[182:183], v[76:77] op_sel:[0,1,0]
	v_pk_fma_f32 v[70:71], v[154:155], v[182:183], v[70:71] op_sel_hi:[1,0,1]
	v_pk_fma_f32 v[74:75], v[154:155], v[182:183], v[74:75] op_sel:[0,1,0]
	s_waitcnt lgkmcnt(7)
	ds_read_b64 v[60:61], v81 offset:2432
	v_pk_mul_f32 v[178:179], v[72:73], v[164:165]
	v_pk_mul_f32 v[180:181], v[76:77], v[164:165]
	v_pk_fma_f32 v[178:179], v[70:71], v[162:163], v[178:179]
	v_pk_fma_f32 v[180:181], v[74:75], v[162:163], v[180:181]
	v_add_f32_e32 v184, v178, v179
	v_add_f32_e32 v185, v180, v181
	v_pk_mul_f32 v[72:73], v[72:73], v[168:169]
	v_pk_mul_f32 v[76:77], v[76:77], v[168:169]
	v_add_f32_dpp v184, v184, v184 row_ror:8 row_mask:0xf bank_mask:0xf bound_ctrl:1
	v_add_f32_dpp v185, v185, v185 row_ror:8 row_mask:0xf bank_mask:0xf bound_ctrl:1
	v_pk_mul_f32 v[70:71], v[70:71], v[166:167]
	v_pk_mul_f32 v[74:75], v[74:75], v[166:167]
	v_add_f32_dpp v184, v184, v184 row_ror:4 row_mask:0xf bank_mask:0xf bound_ctrl:1
	v_add_f32_dpp v185, v185, v185 row_ror:4 row_mask:0xf bank_mask:0xf bound_ctrl:1
	v_pk_fma_f32 v[72:73], v[176:177], v[78:79], v[72:73] op_sel_hi:[1,0,1]
	v_pk_fma_f32 v[76:77], v[176:177], v[78:79], v[76:77] op_sel:[0,1,0]
	v_add_f32_dpp v184, v184, v184 row_ror:2 row_mask:0xf bank_mask:0xf bound_ctrl:1
	v_add_f32_dpp v185, v185, v185 row_ror:2 row_mask:0xf bank_mask:0xf bound_ctrl:1
	v_pk_fma_f32 v[70:71], v[174:175], v[78:79], v[70:71] op_sel_hi:[1,0,1]
	v_pk_fma_f32 v[74:75], v[174:175], v[78:79], v[74:75] op_sel:[0,1,0]
	v_add_f32_dpp v184, v184, v184 row_ror:1 row_mask:0xf bank_mask:0xf bound_ctrl:1
	v_add_f32_dpp v185, v185, v185 row_ror:1 row_mask:0xf bank_mask:0xf bound_ctrl:1
	ds_read_b128 v[56:59], v80 offset:19456
	ds_read_b128 v[150:153], v80 offset:19712
	ds_read_b128 v[154:157], v80 offset:19968
	ds_read_b128 v[158:161], v80 offset:20224
	ds_write_b64 v2, v[184:185] offset:2176
	v_pk_fma_f32 v[72:73], v[172:173], v[184:185], v[72:73] op_sel_hi:[1,0,1]
	v_pk_fma_f32 v[76:77], v[172:173], v[184:185], v[76:77] op_sel:[0,1,0]
	v_pk_fma_f32 v[70:71], v[170:171], v[184:185], v[70:71] op_sel_hi:[1,0,1]
	v_pk_fma_f32 v[74:75], v[170:171], v[184:185], v[74:75] op_sel:[0,1,0]
	s_waitcnt lgkmcnt(7)
	ds_read_b64 v[78:79], v81 offset:2560
	v_pk_mul_f32 v[178:179], v[72:73], v[40:41]
	v_pk_mul_f32 v[180:181], v[76:77], v[40:41]
	v_pk_fma_f32 v[178:179], v[70:71], v[38:39], v[178:179]
	v_pk_fma_f32 v[180:181], v[74:75], v[38:39], v[180:181]
	v_add_f32_e32 v182, v178, v179
	v_add_f32_e32 v183, v180, v181
	v_pk_mul_f32 v[72:73], v[72:73], v[44:45]
	v_pk_mul_f32 v[76:77], v[76:77], v[44:45]
	v_add_f32_dpp v182, v182, v182 row_ror:8 row_mask:0xf bank_mask:0xf bound_ctrl:1
	v_add_f32_dpp v183, v183, v183 row_ror:8 row_mask:0xf bank_mask:0xf bound_ctrl:1
	v_pk_mul_f32 v[70:71], v[70:71], v[42:43]
	v_pk_mul_f32 v[74:75], v[74:75], v[42:43]
	v_add_f32_dpp v182, v182, v182 row_ror:4 row_mask:0xf bank_mask:0xf bound_ctrl:1
	v_add_f32_dpp v183, v183, v183 row_ror:4 row_mask:0xf bank_mask:0xf bound_ctrl:1
	v_pk_fma_f32 v[72:73], v[52:53], v[54:55], v[72:73] op_sel_hi:[1,0,1]
	v_pk_fma_f32 v[76:77], v[52:53], v[54:55], v[76:77] op_sel:[0,1,0]
	v_add_f32_dpp v182, v182, v182 row_ror:2 row_mask:0xf bank_mask:0xf bound_ctrl:1
	v_add_f32_dpp v183, v183, v183 row_ror:2 row_mask:0xf bank_mask:0xf bound_ctrl:1
	v_pk_fma_f32 v[70:71], v[50:51], v[54:55], v[70:71] op_sel_hi:[1,0,1]
	v_pk_fma_f32 v[74:75], v[50:51], v[54:55], v[74:75] op_sel:[0,1,0]
	v_add_f32_dpp v182, v182, v182 row_ror:1 row_mask:0xf bank_mask:0xf bound_ctrl:1
	v_add_f32_dpp v183, v183, v183 row_ror:1 row_mask:0xf bank_mask:0xf bound_ctrl:1
	ds_read_b128 v[162:165], v80 offset:20480
	ds_read_b128 v[166:169], v80 offset:20736
	ds_read_b128 v[170:173], v80 offset:20992
	ds_read_b128 v[174:177], v80 offset:21248
	ds_write_b64 v2, v[182:183] offset:2304
	v_pk_fma_f32 v[72:73], v[48:49], v[182:183], v[72:73] op_sel_hi:[1,0,1]
	v_pk_fma_f32 v[76:77], v[48:49], v[182:183], v[76:77] op_sel:[0,1,0]
	v_pk_fma_f32 v[70:71], v[46:47], v[182:183], v[70:71] op_sel_hi:[1,0,1]
	v_pk_fma_f32 v[74:75], v[46:47], v[182:183], v[74:75] op_sel:[0,1,0]
	s_waitcnt lgkmcnt(7)
	ds_read_b64 v[54:55], v81 offset:2688
	v_pk_mul_f32 v[178:179], v[72:73], v[58:59]
	v_pk_mul_f32 v[180:181], v[76:77], v[58:59]
	v_pk_fma_f32 v[178:179], v[70:71], v[56:57], v[178:179]
	v_pk_fma_f32 v[180:181], v[74:75], v[56:57], v[180:181]
	v_add_f32_e32 v184, v178, v179
	v_add_f32_e32 v185, v180, v181
	v_pk_mul_f32 v[72:73], v[72:73], v[152:153]
	v_pk_mul_f32 v[76:77], v[76:77], v[152:153]
	v_add_f32_dpp v184, v184, v184 row_ror:8 row_mask:0xf bank_mask:0xf bound_ctrl:1
	v_add_f32_dpp v185, v185, v185 row_ror:8 row_mask:0xf bank_mask:0xf bound_ctrl:1
	v_pk_mul_f32 v[70:71], v[70:71], v[150:151]
	v_pk_mul_f32 v[74:75], v[74:75], v[150:151]
	v_add_f32_dpp v184, v184, v184 row_ror:4 row_mask:0xf bank_mask:0xf bound_ctrl:1
	v_add_f32_dpp v185, v185, v185 row_ror:4 row_mask:0xf bank_mask:0xf bound_ctrl:1
	v_pk_fma_f32 v[72:73], v[160:161], v[60:61], v[72:73] op_sel_hi:[1,0,1]
	v_pk_fma_f32 v[76:77], v[160:161], v[60:61], v[76:77] op_sel:[0,1,0]
	v_add_f32_dpp v184, v184, v184 row_ror:2 row_mask:0xf bank_mask:0xf bound_ctrl:1
	v_add_f32_dpp v185, v185, v185 row_ror:2 row_mask:0xf bank_mask:0xf bound_ctrl:1
	v_pk_fma_f32 v[70:71], v[158:159], v[60:61], v[70:71] op_sel_hi:[1,0,1]
	v_pk_fma_f32 v[74:75], v[158:159], v[60:61], v[74:75] op_sel:[0,1,0]
	v_add_f32_dpp v184, v184, v184 row_ror:1 row_mask:0xf bank_mask:0xf bound_ctrl:1
	v_add_f32_dpp v185, v185, v185 row_ror:1 row_mask:0xf bank_mask:0xf bound_ctrl:1
	ds_read_b128 v[38:41], v80 offset:21504
	ds_read_b128 v[42:45], v80 offset:21760
	ds_read_b128 v[46:49], v80 offset:22016
	ds_read_b128 v[50:53], v80 offset:22272
	ds_write_b64 v2, v[184:185] offset:2432
	v_pk_fma_f32 v[72:73], v[156:157], v[184:185], v[72:73] op_sel_hi:[1,0,1]
	v_pk_fma_f32 v[76:77], v[156:157], v[184:185], v[76:77] op_sel:[0,1,0]
	v_pk_fma_f32 v[70:71], v[154:155], v[184:185], v[70:71] op_sel_hi:[1,0,1]
	v_pk_fma_f32 v[74:75], v[154:155], v[184:185], v[74:75] op_sel:[0,1,0]
	s_waitcnt lgkmcnt(7)
	ds_read_b64 v[60:61], v81 offset:2816
	v_pk_mul_f32 v[178:179], v[72:73], v[164:165]
	v_pk_mul_f32 v[180:181], v[76:77], v[164:165]
	v_pk_fma_f32 v[178:179], v[70:71], v[162:163], v[178:179]
	v_pk_fma_f32 v[180:181], v[74:75], v[162:163], v[180:181]
	v_add_f32_e32 v182, v178, v179
	v_add_f32_e32 v183, v180, v181
	v_pk_mul_f32 v[72:73], v[72:73], v[168:169]
	v_pk_mul_f32 v[76:77], v[76:77], v[168:169]
	v_add_f32_dpp v182, v182, v182 row_ror:8 row_mask:0xf bank_mask:0xf bound_ctrl:1
	v_add_f32_dpp v183, v183, v183 row_ror:8 row_mask:0xf bank_mask:0xf bound_ctrl:1
	v_pk_mul_f32 v[70:71], v[70:71], v[166:167]
	v_pk_mul_f32 v[74:75], v[74:75], v[166:167]
	v_add_f32_dpp v182, v182, v182 row_ror:4 row_mask:0xf bank_mask:0xf bound_ctrl:1
	v_add_f32_dpp v183, v183, v183 row_ror:4 row_mask:0xf bank_mask:0xf bound_ctrl:1
	v_pk_fma_f32 v[72:73], v[176:177], v[78:79], v[72:73] op_sel_hi:[1,0,1]
	v_pk_fma_f32 v[76:77], v[176:177], v[78:79], v[76:77] op_sel:[0,1,0]
	v_add_f32_dpp v182, v182, v182 row_ror:2 row_mask:0xf bank_mask:0xf bound_ctrl:1
	v_add_f32_dpp v183, v183, v183 row_ror:2 row_mask:0xf bank_mask:0xf bound_ctrl:1
	v_pk_fma_f32 v[70:71], v[174:175], v[78:79], v[70:71] op_sel_hi:[1,0,1]
	v_pk_fma_f32 v[74:75], v[174:175], v[78:79], v[74:75] op_sel:[0,1,0]
	v_add_f32_dpp v182, v182, v182 row_ror:1 row_mask:0xf bank_mask:0xf bound_ctrl:1
	v_add_f32_dpp v183, v183, v183 row_ror:1 row_mask:0xf bank_mask:0xf bound_ctrl:1
	ds_read_b128 v[56:59], v80 offset:22528
	ds_read_b128 v[150:153], v80 offset:22784
	ds_read_b128 v[154:157], v80 offset:23040
	ds_read_b128 v[158:161], v80 offset:23296
	ds_write_b64 v2, v[182:183] offset:2560
	v_pk_fma_f32 v[72:73], v[172:173], v[182:183], v[72:73] op_sel_hi:[1,0,1]
	v_pk_fma_f32 v[76:77], v[172:173], v[182:183], v[76:77] op_sel:[0,1,0]
	v_pk_fma_f32 v[70:71], v[170:171], v[182:183], v[70:71] op_sel_hi:[1,0,1]
	v_pk_fma_f32 v[74:75], v[170:171], v[182:183], v[74:75] op_sel:[0,1,0]
	s_waitcnt lgkmcnt(7)
	ds_read_b64 v[78:79], v81 offset:2944
	v_pk_mul_f32 v[178:179], v[72:73], v[40:41]
	v_pk_mul_f32 v[180:181], v[76:77], v[40:41]
	v_pk_fma_f32 v[178:179], v[70:71], v[38:39], v[178:179]
	v_pk_fma_f32 v[180:181], v[74:75], v[38:39], v[180:181]
	v_add_f32_e32 v184, v178, v179
	v_add_f32_e32 v185, v180, v181
	v_pk_mul_f32 v[72:73], v[72:73], v[44:45]
	v_pk_mul_f32 v[76:77], v[76:77], v[44:45]
	v_add_f32_dpp v184, v184, v184 row_ror:8 row_mask:0xf bank_mask:0xf bound_ctrl:1
	v_add_f32_dpp v185, v185, v185 row_ror:8 row_mask:0xf bank_mask:0xf bound_ctrl:1
	v_pk_mul_f32 v[70:71], v[70:71], v[42:43]
	v_pk_mul_f32 v[74:75], v[74:75], v[42:43]
	v_add_f32_dpp v184, v184, v184 row_ror:4 row_mask:0xf bank_mask:0xf bound_ctrl:1
	v_add_f32_dpp v185, v185, v185 row_ror:4 row_mask:0xf bank_mask:0xf bound_ctrl:1
	v_pk_fma_f32 v[72:73], v[52:53], v[54:55], v[72:73] op_sel_hi:[1,0,1]
	v_pk_fma_f32 v[76:77], v[52:53], v[54:55], v[76:77] op_sel:[0,1,0]
	v_add_f32_dpp v184, v184, v184 row_ror:2 row_mask:0xf bank_mask:0xf bound_ctrl:1
	v_add_f32_dpp v185, v185, v185 row_ror:2 row_mask:0xf bank_mask:0xf bound_ctrl:1
	v_pk_fma_f32 v[70:71], v[50:51], v[54:55], v[70:71] op_sel_hi:[1,0,1]
	v_pk_fma_f32 v[74:75], v[50:51], v[54:55], v[74:75] op_sel:[0,1,0]
	v_add_f32_dpp v184, v184, v184 row_ror:1 row_mask:0xf bank_mask:0xf bound_ctrl:1
	v_add_f32_dpp v185, v185, v185 row_ror:1 row_mask:0xf bank_mask:0xf bound_ctrl:1
	ds_read_b128 v[162:165], v80 offset:23552
	ds_read_b128 v[166:169], v80 offset:23808
	ds_read_b128 v[170:173], v80 offset:24064
	ds_read_b128 v[174:177], v80 offset:24320
	ds_write_b64 v2, v[184:185] offset:2688
	v_pk_fma_f32 v[72:73], v[48:49], v[184:185], v[72:73] op_sel_hi:[1,0,1]
	v_pk_fma_f32 v[76:77], v[48:49], v[184:185], v[76:77] op_sel:[0,1,0]
	v_pk_fma_f32 v[70:71], v[46:47], v[184:185], v[70:71] op_sel_hi:[1,0,1]
	v_pk_fma_f32 v[74:75], v[46:47], v[184:185], v[74:75] op_sel:[0,1,0]
	s_waitcnt lgkmcnt(7)
	ds_read_b64 v[54:55], v81 offset:3072
	v_pk_mul_f32 v[178:179], v[72:73], v[58:59]
	v_pk_mul_f32 v[180:181], v[76:77], v[58:59]
	v_pk_fma_f32 v[178:179], v[70:71], v[56:57], v[178:179]
	v_pk_fma_f32 v[180:181], v[74:75], v[56:57], v[180:181]
	v_add_f32_e32 v182, v178, v179
	v_add_f32_e32 v183, v180, v181
	v_pk_mul_f32 v[72:73], v[72:73], v[152:153]
	v_pk_mul_f32 v[76:77], v[76:77], v[152:153]
	v_add_f32_dpp v182, v182, v182 row_ror:8 row_mask:0xf bank_mask:0xf bound_ctrl:1
	v_add_f32_dpp v183, v183, v183 row_ror:8 row_mask:0xf bank_mask:0xf bound_ctrl:1
	v_pk_mul_f32 v[70:71], v[70:71], v[150:151]
	v_pk_mul_f32 v[74:75], v[74:75], v[150:151]
	v_add_f32_dpp v182, v182, v182 row_ror:4 row_mask:0xf bank_mask:0xf bound_ctrl:1
	v_add_f32_dpp v183, v183, v183 row_ror:4 row_mask:0xf bank_mask:0xf bound_ctrl:1
	v_pk_fma_f32 v[72:73], v[160:161], v[60:61], v[72:73] op_sel_hi:[1,0,1]
	v_pk_fma_f32 v[76:77], v[160:161], v[60:61], v[76:77] op_sel:[0,1,0]
	v_add_f32_dpp v182, v182, v182 row_ror:2 row_mask:0xf bank_mask:0xf bound_ctrl:1
	v_add_f32_dpp v183, v183, v183 row_ror:2 row_mask:0xf bank_mask:0xf bound_ctrl:1
	v_pk_fma_f32 v[70:71], v[158:159], v[60:61], v[70:71] op_sel_hi:[1,0,1]
	v_pk_fma_f32 v[74:75], v[158:159], v[60:61], v[74:75] op_sel:[0,1,0]
	v_add_f32_dpp v182, v182, v182 row_ror:1 row_mask:0xf bank_mask:0xf bound_ctrl:1
	v_add_f32_dpp v183, v183, v183 row_ror:1 row_mask:0xf bank_mask:0xf bound_ctrl:1
	ds_read_b128 v[38:41], v80 offset:24576
	ds_read_b128 v[42:45], v80 offset:24832
	ds_read_b128 v[46:49], v80 offset:25088
	ds_read_b128 v[50:53], v80 offset:25344
	ds_write_b64 v2, v[182:183] offset:2816
	v_pk_fma_f32 v[72:73], v[156:157], v[182:183], v[72:73] op_sel_hi:[1,0,1]
	v_pk_fma_f32 v[76:77], v[156:157], v[182:183], v[76:77] op_sel:[0,1,0]
	v_pk_fma_f32 v[70:71], v[154:155], v[182:183], v[70:71] op_sel_hi:[1,0,1]
	v_pk_fma_f32 v[74:75], v[154:155], v[182:183], v[74:75] op_sel:[0,1,0]
	s_waitcnt lgkmcnt(7)
	ds_read_b64 v[60:61], v81 offset:3200
	v_pk_mul_f32 v[178:179], v[72:73], v[164:165]
	v_pk_mul_f32 v[180:181], v[76:77], v[164:165]
	v_pk_fma_f32 v[178:179], v[70:71], v[162:163], v[178:179]
	v_pk_fma_f32 v[180:181], v[74:75], v[162:163], v[180:181]
	v_add_f32_e32 v184, v178, v179
	v_add_f32_e32 v185, v180, v181
	v_pk_mul_f32 v[72:73], v[72:73], v[168:169]
	v_pk_mul_f32 v[76:77], v[76:77], v[168:169]
	v_add_f32_dpp v184, v184, v184 row_ror:8 row_mask:0xf bank_mask:0xf bound_ctrl:1
	v_add_f32_dpp v185, v185, v185 row_ror:8 row_mask:0xf bank_mask:0xf bound_ctrl:1
	v_pk_mul_f32 v[70:71], v[70:71], v[166:167]
	v_pk_mul_f32 v[74:75], v[74:75], v[166:167]
	v_add_f32_dpp v184, v184, v184 row_ror:4 row_mask:0xf bank_mask:0xf bound_ctrl:1
	v_add_f32_dpp v185, v185, v185 row_ror:4 row_mask:0xf bank_mask:0xf bound_ctrl:1
	v_pk_fma_f32 v[72:73], v[176:177], v[78:79], v[72:73] op_sel_hi:[1,0,1]
	v_pk_fma_f32 v[76:77], v[176:177], v[78:79], v[76:77] op_sel:[0,1,0]
	v_add_f32_dpp v184, v184, v184 row_ror:2 row_mask:0xf bank_mask:0xf bound_ctrl:1
	v_add_f32_dpp v185, v185, v185 row_ror:2 row_mask:0xf bank_mask:0xf bound_ctrl:1
	v_pk_fma_f32 v[70:71], v[174:175], v[78:79], v[70:71] op_sel_hi:[1,0,1]
	v_pk_fma_f32 v[74:75], v[174:175], v[78:79], v[74:75] op_sel:[0,1,0]
	v_add_f32_dpp v184, v184, v184 row_ror:1 row_mask:0xf bank_mask:0xf bound_ctrl:1
	v_add_f32_dpp v185, v185, v185 row_ror:1 row_mask:0xf bank_mask:0xf bound_ctrl:1
	ds_read_b128 v[56:59], v80 offset:25600
	ds_read_b128 v[150:153], v80 offset:25856
	ds_read_b128 v[154:157], v80 offset:26112
	ds_read_b128 v[158:161], v80 offset:26368
	ds_write_b64 v2, v[184:185] offset:2944
	v_pk_fma_f32 v[72:73], v[172:173], v[184:185], v[72:73] op_sel_hi:[1,0,1]
	v_pk_fma_f32 v[76:77], v[172:173], v[184:185], v[76:77] op_sel:[0,1,0]
	v_pk_fma_f32 v[70:71], v[170:171], v[184:185], v[70:71] op_sel_hi:[1,0,1]
	v_pk_fma_f32 v[74:75], v[170:171], v[184:185], v[74:75] op_sel:[0,1,0]
	s_waitcnt lgkmcnt(7)
	ds_read_b64 v[78:79], v81 offset:3328
	v_pk_mul_f32 v[178:179], v[72:73], v[40:41]
	v_pk_mul_f32 v[180:181], v[76:77], v[40:41]
	v_pk_fma_f32 v[178:179], v[70:71], v[38:39], v[178:179]
	v_pk_fma_f32 v[180:181], v[74:75], v[38:39], v[180:181]
	v_add_f32_e32 v182, v178, v179
	v_add_f32_e32 v183, v180, v181
	v_pk_mul_f32 v[72:73], v[72:73], v[44:45]
	v_pk_mul_f32 v[76:77], v[76:77], v[44:45]
	v_add_f32_dpp v182, v182, v182 row_ror:8 row_mask:0xf bank_mask:0xf bound_ctrl:1
	v_add_f32_dpp v183, v183, v183 row_ror:8 row_mask:0xf bank_mask:0xf bound_ctrl:1
	v_pk_mul_f32 v[70:71], v[70:71], v[42:43]
	v_pk_mul_f32 v[74:75], v[74:75], v[42:43]
	v_add_f32_dpp v182, v182, v182 row_ror:4 row_mask:0xf bank_mask:0xf bound_ctrl:1
	v_add_f32_dpp v183, v183, v183 row_ror:4 row_mask:0xf bank_mask:0xf bound_ctrl:1
	v_pk_fma_f32 v[72:73], v[52:53], v[54:55], v[72:73] op_sel_hi:[1,0,1]
	v_pk_fma_f32 v[76:77], v[52:53], v[54:55], v[76:77] op_sel:[0,1,0]
	v_add_f32_dpp v182, v182, v182 row_ror:2 row_mask:0xf bank_mask:0xf bound_ctrl:1
	v_add_f32_dpp v183, v183, v183 row_ror:2 row_mask:0xf bank_mask:0xf bound_ctrl:1
	v_pk_fma_f32 v[70:71], v[50:51], v[54:55], v[70:71] op_sel_hi:[1,0,1]
	v_pk_fma_f32 v[74:75], v[50:51], v[54:55], v[74:75] op_sel:[0,1,0]
	v_add_f32_dpp v182, v182, v182 row_ror:1 row_mask:0xf bank_mask:0xf bound_ctrl:1
	v_add_f32_dpp v183, v183, v183 row_ror:1 row_mask:0xf bank_mask:0xf bound_ctrl:1
	ds_read_b128 v[162:165], v80 offset:26624
	ds_read_b128 v[166:169], v80 offset:26880
	ds_read_b128 v[170:173], v80 offset:27136
	ds_read_b128 v[174:177], v80 offset:27392
	ds_write_b64 v2, v[182:183] offset:3072
	v_pk_fma_f32 v[72:73], v[48:49], v[182:183], v[72:73] op_sel_hi:[1,0,1]
	v_pk_fma_f32 v[76:77], v[48:49], v[182:183], v[76:77] op_sel:[0,1,0]
	v_pk_fma_f32 v[70:71], v[46:47], v[182:183], v[70:71] op_sel_hi:[1,0,1]
	v_pk_fma_f32 v[74:75], v[46:47], v[182:183], v[74:75] op_sel:[0,1,0]
	s_waitcnt lgkmcnt(7)
	ds_read_b64 v[54:55], v81 offset:3456
	v_pk_mul_f32 v[178:179], v[72:73], v[58:59]
	v_pk_mul_f32 v[180:181], v[76:77], v[58:59]
	v_pk_fma_f32 v[178:179], v[70:71], v[56:57], v[178:179]
	v_pk_fma_f32 v[180:181], v[74:75], v[56:57], v[180:181]
	v_add_f32_e32 v184, v178, v179
	v_add_f32_e32 v185, v180, v181
	v_pk_mul_f32 v[72:73], v[72:73], v[152:153]
	v_pk_mul_f32 v[76:77], v[76:77], v[152:153]
	v_add_f32_dpp v184, v184, v184 row_ror:8 row_mask:0xf bank_mask:0xf bound_ctrl:1
	v_add_f32_dpp v185, v185, v185 row_ror:8 row_mask:0xf bank_mask:0xf bound_ctrl:1
	v_pk_mul_f32 v[70:71], v[70:71], v[150:151]
	v_pk_mul_f32 v[74:75], v[74:75], v[150:151]
	v_add_f32_dpp v184, v184, v184 row_ror:4 row_mask:0xf bank_mask:0xf bound_ctrl:1
	v_add_f32_dpp v185, v185, v185 row_ror:4 row_mask:0xf bank_mask:0xf bound_ctrl:1
	v_pk_fma_f32 v[72:73], v[160:161], v[60:61], v[72:73] op_sel_hi:[1,0,1]
	v_pk_fma_f32 v[76:77], v[160:161], v[60:61], v[76:77] op_sel:[0,1,0]
	v_add_f32_dpp v184, v184, v184 row_ror:2 row_mask:0xf bank_mask:0xf bound_ctrl:1
	v_add_f32_dpp v185, v185, v185 row_ror:2 row_mask:0xf bank_mask:0xf bound_ctrl:1
	v_pk_fma_f32 v[70:71], v[158:159], v[60:61], v[70:71] op_sel_hi:[1,0,1]
	v_pk_fma_f32 v[74:75], v[158:159], v[60:61], v[74:75] op_sel:[0,1,0]
	v_add_f32_dpp v184, v184, v184 row_ror:1 row_mask:0xf bank_mask:0xf bound_ctrl:1
	v_add_f32_dpp v185, v185, v185 row_ror:1 row_mask:0xf bank_mask:0xf bound_ctrl:1
	ds_read_b128 v[38:41], v80 offset:27648
	ds_read_b128 v[42:45], v80 offset:27904
	ds_read_b128 v[46:49], v80 offset:28160
	ds_read_b128 v[50:53], v80 offset:28416
	ds_write_b64 v2, v[184:185] offset:3200
	v_pk_fma_f32 v[72:73], v[156:157], v[184:185], v[72:73] op_sel_hi:[1,0,1]
	v_pk_fma_f32 v[76:77], v[156:157], v[184:185], v[76:77] op_sel:[0,1,0]
	v_pk_fma_f32 v[70:71], v[154:155], v[184:185], v[70:71] op_sel_hi:[1,0,1]
	v_pk_fma_f32 v[74:75], v[154:155], v[184:185], v[74:75] op_sel:[0,1,0]
	s_waitcnt lgkmcnt(7)
	ds_read_b64 v[60:61], v81 offset:3584
	v_pk_mul_f32 v[178:179], v[72:73], v[164:165]
	v_pk_mul_f32 v[180:181], v[76:77], v[164:165]
	v_pk_fma_f32 v[178:179], v[70:71], v[162:163], v[178:179]
	v_pk_fma_f32 v[180:181], v[74:75], v[162:163], v[180:181]
	v_add_f32_e32 v182, v178, v179
	v_add_f32_e32 v183, v180, v181
	v_pk_mul_f32 v[72:73], v[72:73], v[168:169]
	v_pk_mul_f32 v[76:77], v[76:77], v[168:169]
	v_add_f32_dpp v182, v182, v182 row_ror:8 row_mask:0xf bank_mask:0xf bound_ctrl:1
	v_add_f32_dpp v183, v183, v183 row_ror:8 row_mask:0xf bank_mask:0xf bound_ctrl:1
	v_pk_mul_f32 v[70:71], v[70:71], v[166:167]
	v_pk_mul_f32 v[74:75], v[74:75], v[166:167]
	v_add_f32_dpp v182, v182, v182 row_ror:4 row_mask:0xf bank_mask:0xf bound_ctrl:1
	v_add_f32_dpp v183, v183, v183 row_ror:4 row_mask:0xf bank_mask:0xf bound_ctrl:1
	v_pk_fma_f32 v[72:73], v[176:177], v[78:79], v[72:73] op_sel_hi:[1,0,1]
	v_pk_fma_f32 v[76:77], v[176:177], v[78:79], v[76:77] op_sel:[0,1,0]
	v_add_f32_dpp v182, v182, v182 row_ror:2 row_mask:0xf bank_mask:0xf bound_ctrl:1
	v_add_f32_dpp v183, v183, v183 row_ror:2 row_mask:0xf bank_mask:0xf bound_ctrl:1
	v_pk_fma_f32 v[70:71], v[174:175], v[78:79], v[70:71] op_sel_hi:[1,0,1]
	v_pk_fma_f32 v[74:75], v[174:175], v[78:79], v[74:75] op_sel:[0,1,0]
	v_add_f32_dpp v182, v182, v182 row_ror:1 row_mask:0xf bank_mask:0xf bound_ctrl:1
	v_add_f32_dpp v183, v183, v183 row_ror:1 row_mask:0xf bank_mask:0xf bound_ctrl:1
	ds_read_b128 v[56:59], v80 offset:28672
	ds_read_b128 v[150:153], v80 offset:28928
	ds_read_b128 v[154:157], v80 offset:29184
	ds_read_b128 v[158:161], v80 offset:29440
	ds_write_b64 v2, v[182:183] offset:3328
	v_pk_fma_f32 v[72:73], v[172:173], v[182:183], v[72:73] op_sel_hi:[1,0,1]
	v_pk_fma_f32 v[76:77], v[172:173], v[182:183], v[76:77] op_sel:[0,1,0]
	v_pk_fma_f32 v[70:71], v[170:171], v[182:183], v[70:71] op_sel_hi:[1,0,1]
	v_pk_fma_f32 v[74:75], v[170:171], v[182:183], v[74:75] op_sel:[0,1,0]
	s_waitcnt lgkmcnt(7)
	ds_read_b64 v[78:79], v81 offset:3712
	v_pk_mul_f32 v[178:179], v[72:73], v[40:41]
	v_pk_mul_f32 v[180:181], v[76:77], v[40:41]
	v_pk_fma_f32 v[178:179], v[70:71], v[38:39], v[178:179]
	v_pk_fma_f32 v[180:181], v[74:75], v[38:39], v[180:181]
	v_add_f32_e32 v184, v178, v179
	v_add_f32_e32 v185, v180, v181
	v_pk_mul_f32 v[72:73], v[72:73], v[44:45]
	v_pk_mul_f32 v[76:77], v[76:77], v[44:45]
	v_add_f32_dpp v184, v184, v184 row_ror:8 row_mask:0xf bank_mask:0xf bound_ctrl:1
	v_add_f32_dpp v185, v185, v185 row_ror:8 row_mask:0xf bank_mask:0xf bound_ctrl:1
	v_pk_mul_f32 v[70:71], v[70:71], v[42:43]
	v_pk_mul_f32 v[74:75], v[74:75], v[42:43]
	v_add_f32_dpp v184, v184, v184 row_ror:4 row_mask:0xf bank_mask:0xf bound_ctrl:1
	v_add_f32_dpp v185, v185, v185 row_ror:4 row_mask:0xf bank_mask:0xf bound_ctrl:1
	v_pk_fma_f32 v[72:73], v[52:53], v[54:55], v[72:73] op_sel_hi:[1,0,1]
	v_pk_fma_f32 v[76:77], v[52:53], v[54:55], v[76:77] op_sel:[0,1,0]
	v_add_f32_dpp v184, v184, v184 row_ror:2 row_mask:0xf bank_mask:0xf bound_ctrl:1
	v_add_f32_dpp v185, v185, v185 row_ror:2 row_mask:0xf bank_mask:0xf bound_ctrl:1
	v_pk_fma_f32 v[70:71], v[50:51], v[54:55], v[70:71] op_sel_hi:[1,0,1]
	v_pk_fma_f32 v[74:75], v[50:51], v[54:55], v[74:75] op_sel:[0,1,0]
	v_add_f32_dpp v184, v184, v184 row_ror:1 row_mask:0xf bank_mask:0xf bound_ctrl:1
	v_add_f32_dpp v185, v185, v185 row_ror:1 row_mask:0xf bank_mask:0xf bound_ctrl:1
	ds_read_b128 v[162:165], v80 offset:29696
	ds_read_b128 v[166:169], v80 offset:29952
	ds_read_b128 v[170:173], v80 offset:30208
	ds_read_b128 v[174:177], v80 offset:30464
	ds_write_b64 v2, v[184:185] offset:3456
	v_pk_fma_f32 v[72:73], v[48:49], v[184:185], v[72:73] op_sel_hi:[1,0,1]
	v_pk_fma_f32 v[76:77], v[48:49], v[184:185], v[76:77] op_sel:[0,1,0]
	v_pk_fma_f32 v[70:71], v[46:47], v[184:185], v[70:71] op_sel_hi:[1,0,1]
	v_pk_fma_f32 v[74:75], v[46:47], v[184:185], v[74:75] op_sel:[0,1,0]
	s_waitcnt lgkmcnt(7)
	ds_read_b64 v[54:55], v81 offset:3840
	v_pk_mul_f32 v[178:179], v[72:73], v[58:59]
	v_pk_mul_f32 v[180:181], v[76:77], v[58:59]
	v_pk_fma_f32 v[178:179], v[70:71], v[56:57], v[178:179]
	v_pk_fma_f32 v[180:181], v[74:75], v[56:57], v[180:181]
	v_add_f32_e32 v182, v178, v179
	v_add_f32_e32 v183, v180, v181
	v_pk_mul_f32 v[72:73], v[72:73], v[152:153]
	v_pk_mul_f32 v[76:77], v[76:77], v[152:153]
	v_add_f32_dpp v182, v182, v182 row_ror:8 row_mask:0xf bank_mask:0xf bound_ctrl:1
	v_add_f32_dpp v183, v183, v183 row_ror:8 row_mask:0xf bank_mask:0xf bound_ctrl:1
	v_pk_mul_f32 v[70:71], v[70:71], v[150:151]
	v_pk_mul_f32 v[74:75], v[74:75], v[150:151]
	v_add_f32_dpp v182, v182, v182 row_ror:4 row_mask:0xf bank_mask:0xf bound_ctrl:1
	v_add_f32_dpp v183, v183, v183 row_ror:4 row_mask:0xf bank_mask:0xf bound_ctrl:1
	v_pk_fma_f32 v[72:73], v[160:161], v[60:61], v[72:73] op_sel_hi:[1,0,1]
	v_pk_fma_f32 v[76:77], v[160:161], v[60:61], v[76:77] op_sel:[0,1,0]
	v_add_f32_dpp v182, v182, v182 row_ror:2 row_mask:0xf bank_mask:0xf bound_ctrl:1
	v_add_f32_dpp v183, v183, v183 row_ror:2 row_mask:0xf bank_mask:0xf bound_ctrl:1
	v_pk_fma_f32 v[70:71], v[158:159], v[60:61], v[70:71] op_sel_hi:[1,0,1]
	v_pk_fma_f32 v[74:75], v[158:159], v[60:61], v[74:75] op_sel:[0,1,0]
	v_add_f32_dpp v182, v182, v182 row_ror:1 row_mask:0xf bank_mask:0xf bound_ctrl:1
	v_add_f32_dpp v183, v183, v183 row_ror:1 row_mask:0xf bank_mask:0xf bound_ctrl:1
	ds_read_b128 v[38:41], v80 offset:30720
	ds_read_b128 v[42:45], v80 offset:30976
	ds_read_b128 v[46:49], v80 offset:31232
	ds_read_b128 v[50:53], v80 offset:31488
	ds_write_b64 v2, v[182:183] offset:3584
	v_pk_fma_f32 v[72:73], v[156:157], v[182:183], v[72:73] op_sel_hi:[1,0,1]
	v_pk_fma_f32 v[76:77], v[156:157], v[182:183], v[76:77] op_sel:[0,1,0]
	v_pk_fma_f32 v[70:71], v[154:155], v[182:183], v[70:71] op_sel_hi:[1,0,1]
	v_pk_fma_f32 v[74:75], v[154:155], v[182:183], v[74:75] op_sel:[0,1,0]
	s_waitcnt lgkmcnt(7)
	ds_read_b64 v[60:61], v81 offset:3968
	v_pk_mul_f32 v[178:179], v[72:73], v[164:165]
	v_pk_mul_f32 v[180:181], v[76:77], v[164:165]
	v_pk_fma_f32 v[178:179], v[70:71], v[162:163], v[178:179]
	v_pk_fma_f32 v[180:181], v[74:75], v[162:163], v[180:181]
	v_add_f32_e32 v184, v178, v179
	v_add_f32_e32 v185, v180, v181
	v_pk_mul_f32 v[72:73], v[72:73], v[168:169]
	v_pk_mul_f32 v[76:77], v[76:77], v[168:169]
	v_add_f32_dpp v184, v184, v184 row_ror:8 row_mask:0xf bank_mask:0xf bound_ctrl:1
	v_add_f32_dpp v185, v185, v185 row_ror:8 row_mask:0xf bank_mask:0xf bound_ctrl:1
	v_pk_mul_f32 v[70:71], v[70:71], v[166:167]
	v_pk_mul_f32 v[74:75], v[74:75], v[166:167]
	v_add_f32_dpp v184, v184, v184 row_ror:4 row_mask:0xf bank_mask:0xf bound_ctrl:1
	v_add_f32_dpp v185, v185, v185 row_ror:4 row_mask:0xf bank_mask:0xf bound_ctrl:1
	v_pk_fma_f32 v[72:73], v[176:177], v[78:79], v[72:73] op_sel_hi:[1,0,1]
	v_pk_fma_f32 v[76:77], v[176:177], v[78:79], v[76:77] op_sel:[0,1,0]
	v_add_f32_dpp v184, v184, v184 row_ror:2 row_mask:0xf bank_mask:0xf bound_ctrl:1
	v_add_f32_dpp v185, v185, v185 row_ror:2 row_mask:0xf bank_mask:0xf bound_ctrl:1
	v_pk_fma_f32 v[70:71], v[174:175], v[78:79], v[70:71] op_sel_hi:[1,0,1]
	v_pk_fma_f32 v[74:75], v[174:175], v[78:79], v[74:75] op_sel:[0,1,0]
	v_add_f32_dpp v184, v184, v184 row_ror:1 row_mask:0xf bank_mask:0xf bound_ctrl:1
	v_add_f32_dpp v185, v185, v185 row_ror:1 row_mask:0xf bank_mask:0xf bound_ctrl:1
	ds_read_b128 v[56:59], v80 offset:31744
	ds_read_b128 v[150:153], v80 offset:32000
	ds_read_b128 v[154:157], v80 offset:32256
	ds_read_b128 v[158:161], v80 offset:32512
	ds_write_b64 v2, v[184:185] offset:3712
	v_pk_fma_f32 v[72:73], v[172:173], v[184:185], v[72:73] op_sel_hi:[1,0,1]
	v_pk_fma_f32 v[76:77], v[172:173], v[184:185], v[76:77] op_sel:[0,1,0]
	v_pk_fma_f32 v[70:71], v[170:171], v[184:185], v[70:71] op_sel_hi:[1,0,1]
	v_pk_fma_f32 v[74:75], v[170:171], v[184:185], v[74:75] op_sel:[0,1,0]
	s_waitcnt lgkmcnt(7)
	v_pk_mul_f32 v[178:179], v[72:73], v[40:41]
	v_pk_mul_f32 v[180:181], v[76:77], v[40:41]
	v_pk_fma_f32 v[178:179], v[70:71], v[38:39], v[178:179]
	v_pk_fma_f32 v[180:181], v[74:75], v[38:39], v[180:181]
	v_add_f32_e32 v182, v178, v179
	v_add_f32_e32 v183, v180, v181
	v_pk_mul_f32 v[72:73], v[72:73], v[44:45]
	v_pk_mul_f32 v[76:77], v[76:77], v[44:45]
	v_add_f32_dpp v182, v182, v182 row_ror:8 row_mask:0xf bank_mask:0xf bound_ctrl:1
	v_add_f32_dpp v183, v183, v183 row_ror:8 row_mask:0xf bank_mask:0xf bound_ctrl:1
	v_pk_mul_f32 v[70:71], v[70:71], v[42:43]
	v_pk_mul_f32 v[74:75], v[74:75], v[42:43]
	v_add_f32_dpp v182, v182, v182 row_ror:4 row_mask:0xf bank_mask:0xf bound_ctrl:1
	v_add_f32_dpp v183, v183, v183 row_ror:4 row_mask:0xf bank_mask:0xf bound_ctrl:1
	v_pk_fma_f32 v[72:73], v[52:53], v[54:55], v[72:73] op_sel_hi:[1,0,1]
	v_pk_fma_f32 v[76:77], v[52:53], v[54:55], v[76:77] op_sel:[0,1,0]
	v_add_f32_dpp v182, v182, v182 row_ror:2 row_mask:0xf bank_mask:0xf bound_ctrl:1
	v_add_f32_dpp v183, v183, v183 row_ror:2 row_mask:0xf bank_mask:0xf bound_ctrl:1
	v_pk_fma_f32 v[70:71], v[50:51], v[54:55], v[70:71] op_sel_hi:[1,0,1]
	v_pk_fma_f32 v[74:75], v[50:51], v[54:55], v[74:75] op_sel:[0,1,0]
	v_add_f32_dpp v182, v182, v182 row_ror:1 row_mask:0xf bank_mask:0xf bound_ctrl:1
	v_add_f32_dpp v183, v183, v183 row_ror:1 row_mask:0xf bank_mask:0xf bound_ctrl:1
	ds_write_b64 v2, v[182:183] offset:3840
	v_pk_fma_f32 v[72:73], v[48:49], v[182:183], v[72:73] op_sel_hi:[1,0,1]
	v_pk_fma_f32 v[76:77], v[48:49], v[182:183], v[76:77] op_sel:[0,1,0]
	v_pk_fma_f32 v[70:71], v[46:47], v[182:183], v[70:71] op_sel_hi:[1,0,1]
	v_pk_fma_f32 v[74:75], v[46:47], v[182:183], v[74:75] op_sel:[0,1,0]
	s_waitcnt lgkmcnt(2)
	v_pk_mul_f32 v[178:179], v[72:73], v[58:59]
	v_pk_mul_f32 v[180:181], v[76:77], v[58:59]
	v_pk_fma_f32 v[178:179], v[70:71], v[56:57], v[178:179]
	v_pk_fma_f32 v[180:181], v[74:75], v[56:57], v[180:181]
	v_add_f32_e32 v184, v178, v179
	v_add_f32_e32 v185, v180, v181
	v_pk_mul_f32 v[72:73], v[72:73], v[152:153]
	v_pk_mul_f32 v[76:77], v[76:77], v[152:153]
	v_add_f32_dpp v184, v184, v184 row_ror:8 row_mask:0xf bank_mask:0xf bound_ctrl:1
	v_add_f32_dpp v185, v185, v185 row_ror:8 row_mask:0xf bank_mask:0xf bound_ctrl:1
	v_pk_mul_f32 v[70:71], v[70:71], v[150:151]
	v_pk_mul_f32 v[74:75], v[74:75], v[150:151]
	v_add_f32_dpp v184, v184, v184 row_ror:4 row_mask:0xf bank_mask:0xf bound_ctrl:1
	v_add_f32_dpp v185, v185, v185 row_ror:4 row_mask:0xf bank_mask:0xf bound_ctrl:1
	v_pk_fma_f32 v[72:73], v[160:161], v[60:61], v[72:73] op_sel_hi:[1,0,1]
	v_pk_fma_f32 v[76:77], v[160:161], v[60:61], v[76:77] op_sel:[0,1,0]
	v_add_f32_dpp v184, v184, v184 row_ror:2 row_mask:0xf bank_mask:0xf bound_ctrl:1
	v_add_f32_dpp v185, v185, v185 row_ror:2 row_mask:0xf bank_mask:0xf bound_ctrl:1
	v_pk_fma_f32 v[70:71], v[158:159], v[60:61], v[70:71] op_sel_hi:[1,0,1]
	v_pk_fma_f32 v[74:75], v[158:159], v[60:61], v[74:75] op_sel:[0,1,0]
	v_add_f32_dpp v184, v184, v184 row_ror:1 row_mask:0xf bank_mask:0xf bound_ctrl:1
	v_add_f32_dpp v185, v185, v185 row_ror:1 row_mask:0xf bank_mask:0xf bound_ctrl:1
	ds_write_b64 v2, v[184:185] offset:3968
	v_pk_fma_f32 v[72:73], v[156:157], v[184:185], v[72:73] op_sel_hi:[1,0,1]
	v_pk_fma_f32 v[76:77], v[156:157], v[184:185], v[76:77] op_sel:[0,1,0]
	v_pk_fma_f32 v[70:71], v[154:155], v[184:185], v[70:71] op_sel_hi:[1,0,1]
	v_pk_fma_f32 v[74:75], v[154:155], v[184:185], v[74:75] op_sel:[0,1,0]
	s_setprio 0
	s_branch .LBB0_483
